# na_v part of VT stored fragment-major by the transposer phase so the NA attention V operand loads are 1 KB contiguous per wave; gla_c finish-section loads hoisted; plus KVS fragment-major layout and N
# speedup vs baseline: 1.0093x; 1.0039x over previous
.LBB0_730:
	s_mul_hi_i32 s12, s4, 0x1948b0fd
	s_lshr_b32 s13, s12, 31
	s_ashr_i32 s12, s12, 7
	s_mul_hi_i32 s4, s4, 0x38e38e39
	s_add_i32 s13, s12, s13
	s_lshr_b32 s12, s4, 31
	s_ashr_i32 s4, s4, 3
	s_add_i32 s4, s4, s12
	s_mul_hi_i32 s12, s4, 0x38e38e39
	s_lshr_b32 s16, s12, 31
	s_lshr_b32 s12, s12, 3
	s_add_i32 s12, s12, s16
	s_mul_i32 s12, s12, 36
	s_sub_i32 s12, s4, s12
	s_mov_b32 s100, s12
	s_mov_b32 s101, s13
	s_barrier
	ds_write_b128 v13, v[0:3]
	s_waitcnt lgkmcnt(0)
	s_barrier
	ds_read_u16 v0, v12
	ds_read_u16 v1, v12 offset:144
	ds_read_u16 v2, v12 offset:288
	ds_read_u16 v3, v12 offset:432
	ds_read_u16 v11, v12 offset:576
	ds_read_u16 v14, v12 offset:720
	ds_read_u16 v15, v12 offset:864
	ds_read_u16 v16, v12 offset:1008
	s_lshl_b32 s16, s12, 6
	s_mulk_i32 s4, 0xf700
	s_add_i32 s12, s5, s4
	s_mul_hi_i32 s4, s13, 0x900
	s_mulk_i32 s13, 0x900
	s_ashr_i32 s17, s16, 31
	s_add_u32 s16, s16, s13
	s_addc_u32 s17, s17, s4
	s_waitcnt lgkmcnt(6)
	v_lshl_or_b32 v0, v1, 16, v0
	s_waitcnt lgkmcnt(4)
	v_lshl_or_b32 v1, v3, 16, v2
	s_waitcnt lgkmcnt(2)
	v_lshl_or_b32 v2, v14, 16, v11
	s_waitcnt lgkmcnt(0)
	v_lshl_or_b32 v3, v16, 16, v15
	v_lshl_add_u64 v[14:15], s[16:17], 0, v[8:9]
	v_mov_b64_e32 v[16:17], s[8:9]
	v_mad_u64_u32 v[16:17], s[16:17], v14, s75, v[16:17]
	v_mad_i32_i24 v17, v15, s75, v17
	s_ashr_i32 s13, s12, 31
	v_lshl_add_u64 v[14:15], s[12:13], 1, v[16:17]
	v_mov_b32_e32 v11, v97
	v_lshl_add_u64 v[14:15], v[14:15], 0, v[10:11]
	s_cmp_gt_u32 s100, 15
	s_cbranch_scc1 .Lvt_keep
	s_mul_i32 s100, s100, 72
	s_lshr_b32 vcc_lo, s12, 5
	s_add_i32 s100, s100, vcc_lo
	s_lshl_b32 s100, s100, 12
	s_mul_i32 s101, s101, 0xa20000
	s_add_i32 s100, s100, s101
	v_lshrrev_b32_e32 v14, 4, v8
	v_and_b32_e32 v15, 15, v8
	v_lshlrev_b32_e32 v14, 10, v14
	v_lshl_or_b32 v14, v15, 6, v14
	v_and_b32_e32 v15, 48, v10
	v_or_b32_e32 v14, v14, v15
	v_lshrrev_b32_e32 v15, 6, v10
	v_lshl_or_b32 v14, v15, 12, v14
	v_add_u32_e32 v14, s100, v14
	v_mov_b32_e32 v15, v97
	v_lshl_add_u64 v[14:15], s[8:9], 0, v[14:15]
.Lvt_keep:
	global_store_dwordx4 v[14:15], v[0:3], off
	s_add_i32 s5, s5, s14
	s_andn2_b64 vcc, exec, s[10:11]
	s_waitcnt vmcnt(1)
	v_mov_b64_e32 v[0:1], v[4:5]
	v_mov_b64_e32 v[2:3], v[6:7]
	s_mov_b32 s4, s15
	s_cbranch_vccz .LBB0_738

.LBB0_874:
	s_lshl_b32 s76, s4, 7
	v_add_u32_e32 v192, s9, v178
	v_lshl_add_u64 v[194:195], v[182:183], 0, s[76:77]
	v_mad_i64_i32 v[0:1], s[2:3], v192, s59, v[194:195]
	v_add_u32_e32 v190, 16, v192
	global_load_dwordx4 v[56:59], v[0:1], off
	global_load_dwordx4 v[60:63], v[0:1], off offset:64
	v_mad_i64_i32 v[0:1], s[2:3], v190, s59, v[194:195]
	v_add_u32_e32 v188, 32, v192
	global_load_dwordx4 v[64:67], v[0:1], off
	global_load_dwordx4 v[68:71], v[0:1], off offset:64
	v_mad_i64_i32 v[0:1], s[2:3], v188, s59, v[194:195]
	v_add_u32_e32 v186, 48, v192
	global_load_dwordx4 v[72:75], v[0:1], off
	global_load_dwordx4 v[76:79], v[0:1], off offset:64
	v_mad_i64_i32 v[0:1], s[2:3], v186, s59, v[194:195]
	s_lshl_b32 s38, s6, 8
	global_load_dwordx4 v[80:83], v[0:1], off
	global_load_dwordx4 v[84:87], v[0:1], off offset:64
	v_add_u32_e32 v5, s38, v221
	v_mov_b64_e32 v[0:1], s[78:79]
	v_mad_i64_i32 v[2:3], s[2:3], v5, s59, v[0:1]
	v_lshl_add_u64 v[2:3], v[2:3], 0, s[76:77]
	v_lshlrev_b32_e32 v96, 1, v180
	v_lshl_add_u64 v[2:3], v[2:3], 0, v[96:97]
	s_waitcnt vmcnt(0) expcnt(0) lgkmcnt(0)
	global_load_dwordx4 v[158:161], v[2:3], off offset:2048
	global_load_dwordx4 v[154:157], v[2:3], off offset:2112
	v_or_b32_e32 v2, 4, v5
	v_sub_u32_e64 v4, s7, 4 clamp
	v_mad_i64_i32 v[0:1], s[2:3], v2, s59, v[0:1]
	v_readfirstlane_b32 s2, v4
	s_lshl_b32 s34, s4, 6
	v_lshl_add_u64 v[0:1], v[0:1], 0, s[76:77]
	s_min_u32 s35, s2, 24
	s_mul_i32 s3, s6, 0x900
	v_lshl_add_u64 v[0:1], v[0:1], 0, v[96:97]
	s_add_u32 s3, s3, s34
	global_load_dwordx4 v[166:169], v[0:1], off offset:2048
	global_load_dwordx4 v[162:165], v[0:1], off offset:2112
	s_mul_hi_i32 s2, s6, 0x900
	v_mov_b32_e32 v2, s3
	v_mov_b64_e32 v[0:1], s[80:81]
	s_addc_u32 s4, s2, 0
	v_mad_u64_u32 v[196:197], s[2:3], v2, s75, v[0:1]
	v_mov_b32_e32 v0, 0x1200
	v_mad_i32_i24 v197, s4, v0, v197
	v_lshlrev_b32_e32 v0, 6, v178
	v_mov_b32_e32 v1, v97
	v_lshl_add_u64 v[196:197], v[196:197], 0, v[0:1]
	v_lshl_add_u64 v[0:1], v[196:197], 0, v[96:97]
	v_add_co_u32_e32 v2, vcc, 0x40000, v0
	s_mov_b32 s2, 0x40800
	s_nop 0
	v_addc_co_u32_e32 v3, vcc, 0, v1, vcc
	v_add_co_u32_e32 v4, vcc, s2, v0
	s_mov_b32 s2, 0x40c00
	s_nop 0
	v_addc_co_u32_e32 v5, vcc, 0, v1, vcc
	v_add_co_u32_e32 v6, vcc, s2, v0
	s_mov_b32 s2, 0x40400
	s_nop 0
	v_addc_co_u32_e32 v7, vcc, 0, v1, vcc
	v_add_co_u32_e32 v0, vcc, s2, v0
	global_load_dwordx4 v[110:113], v[4:5], off
	global_load_dwordx4 v[106:109], v[6:7], off
	v_addc_co_u32_e32 v1, vcc, 0, v1, vcc
	global_load_dwordx4 v[122:125], v[0:1], off
	global_load_dwordx4 v[134:137], v[2:3], off
	s_mov_b64 s[4:5], 0x400
	v_lshl_add_u64 v[198:199], v[196:197], 0, s[4:5]
	s_mov_b64 s[4:5], 0x800
	v_mov_b32_e32 v98, v97
	v_mov_b32_e32 v99, v97
	v_mov_b32_e32 v100, v97
	v_mov_b32_e32 v101, v97
	v_lshl_add_u64 v[200:201], v[196:197], 0, s[4:5]
	s_mov_b64 s[4:5], 0xc00
	s_lshl_b32 s37, s6, 11
	s_sub_i32 s39, s35, s7
	v_mov_b64_e32 v[104:105], v[100:101]
	v_mov_b64_e32 v[92:93], v[98:99]
	v_mov_b64_e32 v[88:89], v[98:99]
	v_mov_b64_e32 v[52:53], v[98:99]
	v_mov_b64_e32 v[48:49], v[98:99]
	v_mov_b64_e32 v[44:45], v[98:99]
	v_mov_b64_e32 v[40:41], v[98:99]
	v_mov_b64_e32 v[36:37], v[98:99]
	v_mov_b64_e32 v[32:33], v[98:99]
	v_mov_b64_e32 v[28:29], v[98:99]
	v_mov_b64_e32 v[24:25], v[98:99]
	v_mov_b64_e32 v[20:21], v[98:99]
	v_mov_b64_e32 v[16:17], v[98:99]
	v_mov_b64_e32 v[12:13], v[98:99]
	v_mov_b64_e32 v[8:9], v[98:99]
	v_ashrrev_i32_e32 v193, 31, v192
	v_ashrrev_i32_e32 v191, 31, v190
	s_mov_b32 s36, 32
	v_ashrrev_i32_e32 v189, 31, v188
	v_ashrrev_i32_e32 v187, 31, v186
	s_mov_b32 s2, 0
	v_lshl_add_u64 v[202:203], v[196:197], 0, s[4:5]
	s_addk_i32 s37, 0xff00
	s_addk_i32 s38, 0x2000
	s_add_i32 s39, s39, -4
	s_waitcnt vmcnt(7)
	v_mov_b64_e32 v[118:119], v[158:159]
	s_waitcnt vmcnt(6)
	v_mov_b64_e32 v[114:115], v[154:155]
	v_mov_b32_e32 v230, 0
	v_mov_b32_e32 v234, 0xf149f2ca
	v_mov_b32_e32 v235, 0xf149f2ca
	v_mov_b32_e32 v236, 0xf149f2ca
	v_mov_b32_e32 v237, 0xf149f2ca
	v_mov_b32_e32 v231, 0
	v_mov_b32_e32 v232, 0
	v_mov_b32_e32 v233, 0
	v_mov_b64_e32 v[102:103], v[98:99]
	v_mov_b64_e32 v[94:95], v[100:101]
	s_waitcnt vmcnt(5)
	v_mov_b64_e32 v[130:131], v[166:167]
	s_waitcnt vmcnt(4)
	v_mov_b64_e32 v[126:127], v[162:163]
	v_mov_b64_e32 v[90:91], v[100:101]
	v_mov_b64_e32 v[54:55], v[100:101]
	v_mov_b64_e32 v[50:51], v[100:101]
	v_mov_b64_e32 v[46:47], v[100:101]
	v_mov_b64_e32 v[42:43], v[100:101]
	v_mov_b64_e32 v[38:39], v[100:101]
	v_mov_b64_e32 v[34:35], v[100:101]
	v_mov_b64_e32 v[30:31], v[100:101]
	v_mov_b64_e32 v[26:27], v[100:101]
	v_mov_b64_e32 v[22:23], v[100:101]
	v_mov_b64_e32 v[18:19], v[100:101]
	v_mov_b64_e32 v[14:15], v[100:101]
	v_mov_b64_e32 v[10:11], v[100:101]
	v_mov_b64_e32 v[128:129], v[164:165]
	v_mov_b64_e32 v[132:133], v[168:169]
	v_mov_b64_e32 v[116:117], v[156:157]
	v_mov_b64_e32 v[120:121], v[160:161]
	s_waitcnt vmcnt(3)
	v_mov_b64_e32 v[152:153], v[112:113]
	s_waitcnt vmcnt(2)
	v_mov_b64_e32 v[148:149], v[108:109]
	v_mov_b64_e32 v[146:147], v[106:107]
	s_waitcnt vmcnt(1)
	v_mov_b64_e32 v[140:141], v[124:125]
	s_waitcnt vmcnt(0)
	v_mov_b64_e32 v[144:145], v[136:137]
	v_mov_b64_e32 v[150:151], v[110:111]
	v_mov_b64_e32 v[138:139], v[122:123]
	v_mov_b64_e32 v[142:143], v[134:135]
	s_add_i32 s40, s2, 1
	s_cmp_ge_u32 s40, s31
	s_cbranch_scc1 .LBB0_877
	s_branch .LBB0_876

.LBB0_876:
	s_lshr_b32 s3, s40, 1
	s_add_i32 s4, s3, s35
	s_lshl_b32 s4, s4, 6
	s_lshl_b32 s3, s3, 6
	s_and_b32 s6, s36, 32
	s_add_i32 s5, s37, s4
	s_add_i32 s7, s38, s3
	s_add_i32 s8, s4, 0xffffff00
	s_addk_i32 s3, 0x800
	s_cmp_lt_u32 s2, 7
	s_cselect_b32 s4, s7, s5
	v_or_b32_e32 v0, s4, v179
	v_or_b32_e32 v2, s6, v0
	v_mad_i64_i32 v[0:1], s[4:5], v2, s59, v[194:195]
	global_load_dwordx4 v[118:121], v[0:1], off offset:2048
	global_load_dwordx4 v[114:117], v[0:1], off offset:2112
	v_or_b32_e32 v0, 4, v2
	v_mad_i64_i32 v[0:1], s[4:5], v0, s59, v[194:195]
	s_cselect_b32 s4, s3, s8
	s_ashr_i32 s5, s4, 31
	s_lshl_b64 s[4:5], s[4:5], 7
	global_load_dwordx4 v[130:133], v[0:1], off offset:2048
	global_load_dwordx4 v[126:129], v[0:1], off offset:2112
	v_lshl_add_u64 v[0:1], v[196:197], 0, s[4:5]
	s_lshl_b32 s76, s6, 7
	v_lshl_add_u64 v[0:1], v[0:1], 0, s[76:77]
	v_lshl_add_u64 v[2:3], v[198:199], 0, s[4:5]
	v_lshl_add_u64 v[0:1], v[0:1], 0, v[96:97]
	v_lshl_add_u64 v[2:3], v[2:3], 0, s[76:77]
	v_lshl_add_u64 v[2:3], v[2:3], 0, v[96:97]
	global_load_dwordx4 v[142:145], v[0:1], off
	global_load_dwordx4 v[138:141], v[2:3], off
	v_lshl_add_u64 v[0:1], v[200:201], 0, s[4:5]
	v_lshl_add_u64 v[0:1], v[0:1], 0, s[76:77]
	v_lshl_add_u64 v[2:3], v[202:203], 0, s[4:5]
	v_lshl_add_u64 v[0:1], v[0:1], 0, v[96:97]
	v_lshl_add_u64 v[2:3], v[2:3], 0, s[76:77]
	v_lshl_add_u64 v[2:3], v[2:3], 0, v[96:97]
	global_load_dwordx4 v[150:153], v[0:1], off
	global_load_dwordx4 v[146:149], v[2:3], off

.LBB0_1053:
	s_or_b64 exec, exec, s[10:11]
	s_waitcnt lgkmcnt(0)
	s_barrier
	ds_read2st64_b32 v[32:33], v63 offset1:1
	v_mov_b64_e32 v[34:35], s[44:45]
	v_mad_i64_i32 v[34:35], s[10:11], v52, s59, v[34:35]
	s_lshl_b32 s76, s8, 1
	s_waitcnt lgkmcnt(0)
	v_add_f32_e32 v32, v32, v33
	v_mov_b32_e32 v33, 0x358637bd
	v_fmamk_f32 v32, v32, 0x3b800000, v33
	v_cmp_gt_f32_e32 vcc, s33, v32
	v_mul_f32_e32 v33, 0x4b800000, v32
	v_lshl_add_u64 v[34:35], v[34:35], 0, s[76:77]
	v_cndmask_b32_e32 v32, v32, v33, vcc
	v_rsq_f32_e32 v32, v32
	v_lshl_add_u64 v[36:37], s[6:7], 0, v[54:55]
	v_lshlrev_b64 v[42:43], 1, v[44:45]
	v_lshl_add_u64 v[40:41], v[36:37], 0, s[76:77]
	v_lshl_add_u64 v[36:37], v[34:35], 0, v[42:43]
	s_mov_b64 s[8:9], 0xbcfa800
	v_mul_f32_e32 v33, 0x45800000, v32
	v_lshl_add_u64 v[34:35], v[36:37], 0, s[8:9]
	s_mov_b32 s8, 0xbcfa000
	v_cndmask_b32_e32 v32, v32, v33, vcc
	v_add_co_u32_e32 v36, vcc, s8, v36
	s_add_i32 s12, s12, s96
	s_nop 0
	v_addc_co_u32_e32 v37, vcc, 0, v37, vcc
	global_load_dwordx2 v[104:105], v[34:35], off
	global_load_dwordx4 v[120:123], v[48:49], off
	global_load_dwordx2 v[106:107], v[34:35], off offset:32
	global_load_dwordx4 v[124:127], v[48:49], off offset:64
	global_load_dwordx2 v[108:109], v[34:35], off offset:64
	global_load_dwordx4 v[128:131], v[48:49], off offset:128
	global_load_dwordx2 v[110:111], v[34:35], off offset:96
	global_load_dwordx4 v[132:135], v[48:49], off offset:192
	global_load_dwordx2 v[112:113], v[34:35], off offset:128
	global_load_dwordx4 v[136:139], v[48:49], off offset:256
	global_load_dwordx2 v[114:115], v[34:35], off offset:160
	global_load_dwordx4 v[140:143], v[48:49], off offset:320
	global_load_dwordx2 v[116:117], v[34:35], off offset:192
	global_load_dwordx4 v[144:147], v[48:49], off offset:384
	global_load_dwordx2 v[118:119], v[34:35], off offset:224
	global_load_dwordx4 v[148:151], v[48:49], off offset:448
	s_nop 0
	s_cmp_lt_i32 s12, s15
	s_waitcnt vmcnt(15)
	v_lshlrev_b32_e32 v54, 16, v104
	v_mul_f32_e32 v33, 0xbfb8aa3b, v54
	v_exp_f32_e32 v33, v33
	v_and_b32_e32 v55, 0xffff0000, v104
	v_add_f32_e32 v33, 1.0, v33
	v_rcp_f32_e32 v56, v33
	v_pk_mul_f32 v[28:29], v[28:29], v[32:33] op_sel_hi:[1,0]
	v_mul_f32_e32 v33, 0xbfb8aa3b, v55
	v_exp_f32_e32 v33, v33
	s_waitcnt vmcnt(14)
	v_pk_mul_f32 v[28:29], v[120:121], v[28:29]
	v_lshlrev_b32_e32 v36, 16, v105
	v_and_b32_e32 v37, 0xffff0000, v105
	v_add_f32_e32 v33, 1.0, v33
	v_rcp_f32_e32 v57, v33
	v_mul_f32_e32 v33, 0xbfb8aa3b, v36
	v_exp_f32_e32 v33, v33
	v_pk_mul_f32 v[28:29], v[28:29], v[54:55]
	v_add_f32_e32 v33, 1.0, v33
	v_rcp_f32_e32 v52, v33
	v_pk_mul_f32 v[30:31], v[30:31], v[32:33] op_sel_hi:[1,0]
	v_mul_f32_e32 v33, 0xbfb8aa3b, v37
	v_exp_f32_e32 v33, v33
	v_pk_mul_f32 v[30:31], v[122:123], v[30:31]
	v_pk_mul_f32 v[28:29], v[56:57], v[28:29]
	v_pk_mul_f32 v[30:31], v[30:31], v[36:37]
	v_add_f32_e32 v33, 1.0, v33
	v_rcp_f32_e32 v53, v33
	v_pk_mul_f32 v[24:25], v[24:25], v[32:33] op_sel_hi:[1,0]
	v_pk_mul_f32 v[36:37], v[52:53], v[30:31]
	v_cvt_pk_bf16_f32 v30, v28, v29
	v_cvt_pk_bf16_f32 v31, v36, v37
	v_lshl_add_u64 v[28:29], v[40:41], 0, v[42:43]
	global_store_dwordx2 v[28:29], v[30:31], off
	s_nop 0
	s_waitcnt vmcnt(14)
	v_lshlrev_b32_e32 v40, 16, v106
	v_and_b32_e32 v41, 0xffff0000, v106
	v_mul_f32_e32 v30, 0xbfb8aa3b, v40
	v_exp_f32_e32 v30, v30
	s_waitcnt vmcnt(13)
	v_pk_mul_f32 v[24:25], v[124:125], v[24:25]
	v_add_f32_e32 v30, 1.0, v30
	v_rcp_f32_e32 v42, v30
	v_mul_f32_e32 v30, 0xbfb8aa3b, v41
	v_exp_f32_e32 v30, v30
	v_pk_mul_f32 v[24:25], v[24:25], v[40:41]
	v_add_f32_e32 v30, 1.0, v30
	v_rcp_f32_e32 v43, v30
	v_lshlrev_b32_e32 v30, 16, v107
	v_mul_f32_e32 v33, 0xbfb8aa3b, v30
	v_exp_f32_e32 v33, v33
	v_and_b32_e32 v31, 0xffff0000, v107
	v_pk_mul_f32 v[24:25], v[24:25], v[42:43]
	v_add_f32_e32 v33, 1.0, v33
	v_pk_mul_f32 v[26:27], v[26:27], v[32:33] op_sel_hi:[1,0]
	v_rcp_f32_e32 v36, v33
	v_pk_mul_f32 v[26:27], v[126:127], v[26:27]
	v_cvt_pk_bf16_f32 v24, v24, v25
	v_pk_mul_f32 v[26:27], v[26:27], v[30:31]
	v_mul_f32_e32 v30, 0xbfb8aa3b, v31
	v_exp_f32_e32 v30, v30
	v_pk_mul_f32 v[20:21], v[20:21], v[32:33] op_sel_hi:[1,0]
	v_pk_mul_f32 v[22:23], v[22:23], v[32:33] op_sel_hi:[1,0]
	v_pk_mul_f32 v[12:13], v[12:13], v[32:33] op_sel_hi:[1,0]
	v_add_f32_e32 v30, 1.0, v30
	v_rcp_f32_e32 v37, v30
	v_pk_mul_f32 v[14:15], v[14:15], v[32:33] op_sel_hi:[1,0]
	v_pk_mul_f32 v[16:17], v[16:17], v[32:33] op_sel_hi:[1,0]
	v_pk_mul_f32 v[18:19], v[18:19], v[32:33] op_sel_hi:[1,0]
	v_pk_mul_f32 v[26:27], v[26:27], v[36:37]
	v_pk_mul_f32 v[8:9], v[8:9], v[32:33] op_sel_hi:[1,0]
	v_cvt_pk_bf16_f32 v25, v26, v27
	global_store_dwordx2 v[28:29], v[24:25], off offset:32
	s_nop 0
	v_pk_mul_f32 v[10:11], v[10:11], v[32:33] op_sel_hi:[1,0]
	v_pk_mul_f32 v[4:5], v[4:5], v[32:33] op_sel_hi:[1,0]
	v_pk_mul_f32 v[6:7], v[6:7], v[32:33] op_sel_hi:[1,0]
	v_pk_mul_f32 v[0:1], v[0:1], v[32:33] op_sel_hi:[1,0]
	v_pk_mul_f32 v[2:3], v[2:3], v[32:33] op_sel_hi:[1,0]
	s_waitcnt vmcnt(13)
	v_and_b32_e32 v37, 0xffff0000, v108
	v_lshlrev_b32_e32 v36, 16, v108
	s_waitcnt vmcnt(12)
	v_pk_mul_f32 v[20:21], v[20:21], v[128:129]
	v_mul_f32_e32 v24, 0xbfb8aa3b, v37
	v_mul_f32_e32 v30, 0xbfb8aa3b, v36
	v_exp_f32_e32 v24, v24
	v_exp_f32_e32 v30, v30
	v_and_b32_e32 v25, 0xffff0000, v109
	v_pk_mul_f32 v[22:23], v[22:23], v[130:131]
	v_add_f32_e32 v24, 1.0, v24
	v_add_f32_e32 v30, 1.0, v30
	v_rcp_f32_e32 v39, v24
	v_lshlrev_b32_e32 v24, 16, v109
	v_rcp_f32_e32 v38, v30
	v_mul_f32_e32 v30, 0xbfb8aa3b, v24
	v_pk_mul_f32 v[22:23], v[22:23], v[24:25]
	v_mul_f32_e32 v24, 0xbfb8aa3b, v25
	v_exp_f32_e32 v30, v30
	v_exp_f32_e32 v24, v24
	v_pk_mul_f32 v[20:21], v[20:21], v[36:37]
	v_add_f32_e32 v30, 1.0, v30
	v_add_f32_e32 v24, 1.0, v24
	v_rcp_f32_e32 v30, v30
	v_rcp_f32_e32 v31, v24
	v_pk_mul_f32 v[20:21], v[20:21], v[38:39]
	v_pk_mul_f32 v[22:23], v[22:23], v[30:31]
	v_cvt_pk_bf16_f32 v20, v20, v21
	v_cvt_pk_bf16_f32 v21, v22, v23
	global_store_dwordx2 v[28:29], v[20:21], off offset:64
	s_nop 0
	s_waitcnt vmcnt(12)
	v_and_b32_e32 v27, 0xffff0000, v110
	v_lshlrev_b32_e32 v26, 16, v110
	s_waitcnt vmcnt(11)
	v_pk_mul_f32 v[12:13], v[12:13], v[132:133]
	v_mul_f32_e32 v20, 0xbfb8aa3b, v27
	v_mul_f32_e32 v24, 0xbfb8aa3b, v26
	v_exp_f32_e32 v20, v20
	v_exp_f32_e32 v24, v24
	v_and_b32_e32 v21, 0xffff0000, v111
	v_pk_mul_f32 v[14:15], v[14:15], v[134:135]
	v_add_f32_e32 v20, 1.0, v20
	v_add_f32_e32 v24, 1.0, v24
	v_rcp_f32_e32 v31, v20
	v_lshlrev_b32_e32 v20, 16, v111
	v_rcp_f32_e32 v30, v24
	v_mul_f32_e32 v24, 0xbfb8aa3b, v20
	v_pk_mul_f32 v[14:15], v[14:15], v[20:21]
	v_mul_f32_e32 v20, 0xbfb8aa3b, v21
	v_exp_f32_e32 v24, v24
	v_exp_f32_e32 v20, v20
	v_pk_mul_f32 v[12:13], v[12:13], v[26:27]
	v_add_f32_e32 v24, 1.0, v24
	v_add_f32_e32 v20, 1.0, v20
	v_rcp_f32_e32 v24, v24
	v_rcp_f32_e32 v25, v20
	v_pk_mul_f32 v[12:13], v[12:13], v[30:31]
	v_pk_mul_f32 v[14:15], v[14:15], v[24:25]
	v_cvt_pk_bf16_f32 v12, v12, v13
	v_cvt_pk_bf16_f32 v13, v14, v15
	global_store_dwordx2 v[28:29], v[12:13], off offset:96
	s_nop 0
	s_waitcnt vmcnt(11)
	v_and_b32_e32 v23, 0xffff0000, v112
	v_lshlrev_b32_e32 v22, 16, v112
	s_waitcnt vmcnt(10)
	v_pk_mul_f32 v[12:13], v[16:17], v[136:137]
	v_mul_f32_e32 v16, 0xbfb8aa3b, v23
	v_mul_f32_e32 v20, 0xbfb8aa3b, v22
	v_exp_f32_e32 v16, v16
	v_exp_f32_e32 v20, v20
	v_and_b32_e32 v17, 0xffff0000, v113
	v_pk_mul_f32 v[14:15], v[18:19], v[138:139]
	v_add_f32_e32 v16, 1.0, v16
	v_add_f32_e32 v20, 1.0, v20
	v_rcp_f32_e32 v25, v16
	v_lshlrev_b32_e32 v16, 16, v113
	v_rcp_f32_e32 v24, v20
	v_mul_f32_e32 v20, 0xbfb8aa3b, v16
	v_pk_mul_f32 v[14:15], v[14:15], v[16:17]
	v_mul_f32_e32 v16, 0xbfb8aa3b, v17
	v_exp_f32_e32 v20, v20
	v_exp_f32_e32 v16, v16
	v_pk_mul_f32 v[12:13], v[12:13], v[22:23]
	v_add_f32_e32 v20, 1.0, v20
	v_add_f32_e32 v16, 1.0, v16
	v_rcp_f32_e32 v20, v20
	v_rcp_f32_e32 v21, v16
	v_pk_mul_f32 v[12:13], v[12:13], v[24:25]
	v_pk_mul_f32 v[14:15], v[14:15], v[20:21]
	v_cvt_pk_bf16_f32 v12, v12, v13
	v_cvt_pk_bf16_f32 v13, v14, v15
	global_store_dwordx2 v[28:29], v[12:13], off offset:128
	s_nop 0
	s_waitcnt vmcnt(10)
	v_and_b32_e32 v19, 0xffff0000, v114
	v_lshlrev_b32_e32 v18, 16, v114
	s_waitcnt vmcnt(9)
	v_pk_mul_f32 v[8:9], v[8:9], v[140:141]
	v_mul_f32_e32 v12, 0xbfb8aa3b, v19
	v_mul_f32_e32 v16, 0xbfb8aa3b, v18
	v_exp_f32_e32 v12, v12
	v_exp_f32_e32 v16, v16
	v_and_b32_e32 v13, 0xffff0000, v115
	v_pk_mul_f32 v[10:11], v[10:11], v[142:143]
	v_add_f32_e32 v12, 1.0, v12
	v_add_f32_e32 v16, 1.0, v16
	v_rcp_f32_e32 v21, v12
	v_lshlrev_b32_e32 v12, 16, v115
	v_rcp_f32_e32 v20, v16
	v_mul_f32_e32 v16, 0xbfb8aa3b, v12
	v_pk_mul_f32 v[10:11], v[10:11], v[12:13]
	v_mul_f32_e32 v12, 0xbfb8aa3b, v13
	v_exp_f32_e32 v16, v16
	v_exp_f32_e32 v12, v12
	v_pk_mul_f32 v[8:9], v[8:9], v[18:19]
	v_add_f32_e32 v16, 1.0, v16
	v_add_f32_e32 v12, 1.0, v12
	v_rcp_f32_e32 v16, v16
	v_rcp_f32_e32 v17, v12
	v_pk_mul_f32 v[8:9], v[8:9], v[20:21]
	v_pk_mul_f32 v[10:11], v[10:11], v[16:17]
	v_cvt_pk_bf16_f32 v8, v8, v9
	v_cvt_pk_bf16_f32 v9, v10, v11
	global_store_dwordx2 v[28:29], v[8:9], off offset:160
	s_nop 0
	s_waitcnt vmcnt(9)
	v_and_b32_e32 v15, 0xffff0000, v116
	v_lshlrev_b32_e32 v14, 16, v116
	s_waitcnt vmcnt(8)
	v_pk_mul_f32 v[4:5], v[4:5], v[144:145]
	v_mul_f32_e32 v8, 0xbfb8aa3b, v15
	v_mul_f32_e32 v12, 0xbfb8aa3b, v14
	v_exp_f32_e32 v8, v8
	v_exp_f32_e32 v12, v12
	v_and_b32_e32 v9, 0xffff0000, v117
	v_pk_mul_f32 v[6:7], v[6:7], v[146:147]
	v_add_f32_e32 v8, 1.0, v8
	v_add_f32_e32 v12, 1.0, v12
	v_rcp_f32_e32 v17, v8
	v_lshlrev_b32_e32 v8, 16, v117
	v_rcp_f32_e32 v16, v12
	v_mul_f32_e32 v12, 0xbfb8aa3b, v8
	v_pk_mul_f32 v[6:7], v[6:7], v[8:9]
	v_mul_f32_e32 v8, 0xbfb8aa3b, v9
	v_exp_f32_e32 v12, v12
	v_exp_f32_e32 v8, v8
	v_pk_mul_f32 v[4:5], v[4:5], v[14:15]
	v_add_f32_e32 v12, 1.0, v12
	v_add_f32_e32 v8, 1.0, v8
	v_rcp_f32_e32 v12, v12
	v_rcp_f32_e32 v13, v8
	v_pk_mul_f32 v[4:5], v[4:5], v[16:17]
	v_pk_mul_f32 v[6:7], v[6:7], v[12:13]
	v_cvt_pk_bf16_f32 v4, v4, v5
	v_cvt_pk_bf16_f32 v5, v6, v7
	global_store_dwordx2 v[28:29], v[4:5], off offset:192
	s_nop 0
	s_waitcnt vmcnt(8)
	v_and_b32_e32 v11, 0xffff0000, v118
	v_lshlrev_b32_e32 v10, 16, v118
	s_waitcnt vmcnt(7)
	v_pk_mul_f32 v[0:1], v[0:1], v[148:149]
	v_mul_f32_e32 v4, 0xbfb8aa3b, v11
	v_mul_f32_e32 v8, 0xbfb8aa3b, v10
	v_exp_f32_e32 v4, v4
	v_exp_f32_e32 v8, v8
	v_and_b32_e32 v5, 0xffff0000, v119
	v_pk_mul_f32 v[2:3], v[2:3], v[150:151]
	v_add_f32_e32 v4, 1.0, v4
	v_add_f32_e32 v8, 1.0, v8
	v_rcp_f32_e32 v13, v4
	v_lshlrev_b32_e32 v4, 16, v119
	v_rcp_f32_e32 v12, v8
	v_mul_f32_e32 v8, 0xbfb8aa3b, v4
	v_pk_mul_f32 v[2:3], v[2:3], v[4:5]
	v_mul_f32_e32 v4, 0xbfb8aa3b, v5
	v_exp_f32_e32 v8, v8
	v_exp_f32_e32 v4, v4
	v_pk_mul_f32 v[0:1], v[0:1], v[10:11]
	v_add_f32_e32 v8, 1.0, v8
	v_add_f32_e32 v4, 1.0, v4
	v_rcp_f32_e32 v8, v8
	v_rcp_f32_e32 v9, v4
	v_pk_mul_f32 v[0:1], v[0:1], v[12:13]
	v_pk_mul_f32 v[2:3], v[2:3], v[8:9]
	v_cvt_pk_bf16_f32 v0, v0, v1
	v_cvt_pk_bf16_f32 v1, v2, v3
	global_store_dwordx2 v[28:29], v[0:1], off offset:224
	s_cbranch_scc0 .LBB0_1062

	.amdhsa_kernel _Z4mega6Params
		.amdhsa_group_segment_fixed_size 0
		.amdhsa_private_segment_fixed_size 0
		.amdhsa_kernarg_size 504
		.amdhsa_user_sgpr_count 2
		.amdhsa_user_sgpr_dispatch_ptr 0
		.amdhsa_user_sgpr_queue_ptr 0
		.amdhsa_user_sgpr_kernarg_segment_ptr 1
		.amdhsa_user_sgpr_dispatch_id 0
		.amdhsa_user_sgpr_kernarg_preload_length 0
		.amdhsa_user_sgpr_kernarg_preload_offset 0
		.amdhsa_user_sgpr_private_segment_size 0
		.amdhsa_uses_dynamic_stack 0
		.amdhsa_enable_private_segment 0
		.amdhsa_system_sgpr_workgroup_id_x 1
		.amdhsa_system_sgpr_workgroup_id_y 0
		.amdhsa_system_sgpr_workgroup_id_z 0
		.amdhsa_system_sgpr_workgroup_info 0
		.amdhsa_system_vgpr_workitem_id 0
		.amdhsa_next_free_vgpr 256
		.amdhsa_next_free_sgpr 102
		.amdhsa_accum_offset 256
		.amdhsa_reserve_vcc 1
		.amdhsa_float_round_mode_32 0
		.amdhsa_float_round_mode_16_64 0
		.amdhsa_float_denorm_mode_32 3
		.amdhsa_float_denorm_mode_16_64 3
		.amdhsa_dx10_clamp 1
		.amdhsa_ieee_mode 1
		.amdhsa_fp16_overflow 0
		.amdhsa_tg_split 0
		.amdhsa_exception_fp_ieee_invalid_op 0
		.amdhsa_exception_fp_denorm_src 0
		.amdhsa_exception_fp_ieee_div_zero 0
		.amdhsa_exception_fp_ieee_overflow 0
		.amdhsa_exception_fp_ieee_underflow 0
		.amdhsa_exception_fp_ieee_inexact 0
		.amdhsa_exception_int_div_zero 0
	.end_amdhsa_kernel

amdhsa.kernels:
  - .agpr_count:     0
    .args:
      - .offset:         0
        .size:           248
        .value_kind:     by_value
      - .offset:         248
        .size:           4
        .value_kind:     hidden_block_count_x
      - .offset:         252
        .size:           4
        .value_kind:     hidden_block_count_y
      - .offset:         256
        .size:           4
        .value_kind:     hidden_block_count_z
      - .offset:         260
        .size:           2
        .value_kind:     hidden_group_size_x
      - .offset:         262
        .size:           2
        .value_kind:     hidden_group_size_y
      - .offset:         264
        .size:           2
        .value_kind:     hidden_group_size_z
      - .offset:         266
        .size:           2
        .value_kind:     hidden_remainder_x
      - .offset:         268
        .size:           2
        .value_kind:     hidden_remainder_y
      - .offset:         270
        .size:           2
        .value_kind:     hidden_remainder_z
      - .offset:         288
        .size:           8
        .value_kind:     hidden_global_offset_x
      - .offset:         296
        .size:           8
        .value_kind:     hidden_global_offset_y
      - .offset:         304
        .size:           8
        .value_kind:     hidden_global_offset_z
      - .offset:         312
        .size:           2
        .value_kind:     hidden_grid_dims
      - .offset:         368
        .size:           4
        .value_kind:     hidden_dynamic_lds_size
    .group_segment_fixed_size: 0
    .kernarg_segment_align: 8
    .kernarg_segment_size: 504
    .language:       OpenCL C
    .language_version:
      - 2
      - 0
    .max_flat_workgroup_size: 512
    .name:           _Z4mega6Params
    .private_segment_fixed_size: 0
    .sgpr_count:     108
    .sgpr_spill_count: 116
    .symbol:         _Z4mega6Params.kd
    .uniform_work_group_size: 1
    .uses_dynamic_stack: false
    .vgpr_count:     256
    .vgpr_spill_count: 0
    .wavefront_size: 64
